# final row loop: per-column constants in LDS swizzled (chunk k of lane l at (k + l/4) mod 4) so the 20 ds_read_b128 per row are bank-conflict free
# speedup vs baseline: 1.0138x; 1.0093x over previous
; #define LAS __attribute__((address_space(3)))
; #define REPS(k) for (int _rep = 0; _rep < ((MK_DUP == (k) || (MK_DUP == 202 && (k) == 0)) ? 2 : 1); ++_rep)
; __device__ __forceinline__ void final_load(RowRaw& R, const bf16_t* __restrict__ tb, const unsigned char* __restrict__ ybuf, const unsigned char* __restrict__ ysh, const float* __restrict__ stats, int row, int lane) {
;     const int c0 = lane * 16;
; #pragma unroll
;     for (int k = 0; k < TOPK; ++k) R.y[k] = __builtin_nontemporal_load((const u32x4*)(ybuf + ((size_t)row * TOPK + k) * D + c0));
;     R.y[8] = __builtin_nontemporal_load((const u32x4*)(ysh + (size_t)row * D + c0));
;     R.t[0] = __builtin_nontemporal_load((const u32x4*)(tb + (size_t)row * D + c0)); R.t[1] = __builtin_nontemporal_load((const u32x4*)(tb + (size_t)row * D + c0 + 8));
;     R.st = *(const f32x2*)(stats + 2 * (size_t)row);
; __global__ void __launch_bounds__(NW * 64, 2) mk_fwd(Args args) {
;     ...
;     REPS(12) if (IN(12)) { PH_BEGIN
;         LAS float* cv = (LAS float*)lds; int curb = -1;
;         for (int c = bx; c < M / 256; c += G) {
;             const int b = c >> 3;
;             if (b != curb) {
;                 __syncthreads();
;                 if (tid < 256) { const int i = tid * 4; *(LAS f32x4*)(cv + i) = *(const f32x4*)(X.ln1_g + i); *(LAS f32x4*)(cv + 1024 + i) = *(const f32x4*)(X.ln1_b + i);
;                     *(LAS f32x4*)(cv + 2048 + i) = *(const f32x4*)(X.ln2_g + i); *(LAS f32x4*)(cv + 3072 + i) = *(const f32x4*)(X.ln2_b + i); *(LAS f32x4*)(cv + 4096 + i) = *(const f32x4*)(mod + b * 6144 + MOD_GATE_F + i); }
;                 __syncthreads(); curb = b;
;             }
;             const int r0 = c * 256 + wave * 32;
;             RowRaw nx; final_load(nx, (const bf16_t*)(ws + WS_TB), ybuf, ws + WS_YSH, (const float*)(ws + WS_STATS), r0, lane);
.LBB0_848:
	s_cmp_lt_i32 s92, 13
	s_cselect_b64 s[0:1], -1, 0
	s_and_b64 s[0:1], s[0:1], s[8:9]
	s_andn2_b64 vcc, exec, s[0:1]
	s_cbranch_vccnz .LBB0_858
	s_mov_b64 s[2:3], s[90:91]
	s_and_b64 vcc, exec, s[96:97]
	s_cbranch_vccnz .LBB0_858
	s_load_dwordx4 s[4:7], s[2:3], 0xa8
	s_load_dword s9, s[90:91], 0xc0
	v_mbcnt_lo_u32_b32 v0, -1, 0
	v_mbcnt_hi_u32_b32 v4, -1, v0
	s_and_b32 s0, s88, 0xffffffc0
	v_mov_b32_e32 v45, 0
	v_add_u32_e32 v2, s0, v4
	s_movk_i32 s0, 0x100
	v_lshlrev_b32_e32 v44, 4, v4
	v_cmp_gt_i32_e64 s[0:1], s0, v2
	v_lshlrev_b32_e32 v0, 2, v2
	v_lshrrev_b32_e32 v204, 4, v2
	v_add_u32_e32 v204, v204, v2
	v_and_b32_e32 v204, 3, v204
	v_and_b32_e32 v205, 0xfc, v2
	v_or_b32_e32 v204, v204, v205
	v_lshlrev_b32_e32 v204, 4, v204
	v_lshrrev_b32_e32 v220, 2, v4
	v_and_b32_e32 v216, 3, v220
	v_lshlrev_b32_e32 v216, 4, v216
	v_lshl_add_u32 v216, v4, 6, v216
	v_add_u32_e32 v217, 1, v220
	v_and_b32_e32 v217, 3, v217
	v_lshlrev_b32_e32 v217, 4, v217
	v_lshl_add_u32 v217, v4, 6, v217
	v_add_u32_e32 v218, 2, v220
	v_and_b32_e32 v218, 3, v218
	v_lshlrev_b32_e32 v218, 4, v218
	v_lshl_add_u32 v218, v4, 6, v218
	v_add_u32_e32 v219, 3, v220
	v_and_b32_e32 v219, 3, v219
	v_lshlrev_b32_e32 v219, 4, v219
	v_lshl_add_u32 v219, v4, 6, v219
	s_waitcnt lgkmcnt(0)
	v_lshl_add_u64 v[2:3], s[6:7], 0, v[44:45]
	s_mov_b64 s[12:13], 0xa000000
	v_lshl_add_u64 v[46:47], v[2:3], 0, s[12:13]
	s_mov_b64 s[12:13], 0x3a000000
	v_lshl_add_u64 v[48:49], v[2:3], 0, s[12:13]
	v_lshlrev_b32_e32 v2, 5, v4
	v_mov_b32_e32 v3, v45
	s_lshl_b32 s11, s89, 5
	v_lshl_add_u64 v[2:3], s[6:7], 0, v[2:3]
	s_mov_b64 s[12:13], 0x32000000
	s_add_u32 s16, s6, 0x1800000
	v_lshl_add_u64 v[50:51], v[2:3], 0, s[12:13]
	v_lshlrev_b32_e32 v2, 6, v4
	v_mov_b32_e32 v3, v45
	v_ashrrev_i32_e32 v1, 31, v0
	s_addc_u32 s17, s7, 0
	v_lshl_add_u64 v[52:53], s[4:5], 0, v[2:3]
	v_lshlrev_b32_e32 v210, 4, v4
	v_mov_b32_e32 v211, 0
	v_lshl_add_u64 v[210:211], s[4:5], 0, v[210:211]
	s_mul_i32 s12, s89, 0x1400
	s_add_i32 s12, s12, 0x8000
	v_mul_u32_u24_e32 v208, 0x50, v4
	v_add_u32_e32 v208, s12, v208
	v_lshrrev_b32_e32 v209, 2, v4
	v_mul_u32_u24_e32 v209, 0x50, v209
	v_and_b32_e32 v212, 3, v4
	v_lshl_add_u32 v209, v212, 4, v209
	v_add_u32_e32 v209, s12, v209
	s_lshl_b32 s4, s44, 8
	s_mov_b32 s22, -1
	s_add_i32 s18, s4, s11
	s_lshl_b32 s19, s9, 8
	v_lshlrev_b64 v[54:55], 2, v[0:1]
	s_movk_i32 s20, 0x1000
	s_mov_b32 s8, 0x3c800000
	s_mov_b32 s10, 0x3f9837f0
	v_mov_b32_e32 v205, 0x3727c5ac
	s_mov_b32 s21, 0xf800000
	v_mov_b32_e32 v206, 0x260

; #define LAS __attribute__((address_space(3)))
; __device__ __forceinline__ void final_row(float* __restrict__ out, const RowRaw& R, const LAS float* cv  , int row, int lane) {
;     asm volatile("" : "+v"(cv));
;     const int c0 = lane * 16;
;     f32x4 a[4], t[4], v[4]; float s = 0.f;
; #pragma unroll
;     for (int j = 0; j < 4; ++j) a[j] = (f32x4){0.f, 0.f, 0.f, 0.f};
; #pragma unroll
;     for (int k = 0; k < 9; ++k) { const unsigned w[4] = {R.y[k].x, R.y[k].y, R.y[k].z, R.y[k].w};
; #pragma unroll
;         for (int j = 0; j < 4; ++j) { const f32x2 lo = __builtin_amdgcn_cvt_pk_f32_fp8((int)w[j], false), hi = __builtin_amdgcn_cvt_pk_f32_fp8((int)w[j], true); a[j].x += lo.x; a[j].y += lo.y; a[j].z += hi.x; a[j].w += hi.y; } }
;     unpack_t16r(R.t[0], R.t[1], t);
; #pragma unroll
;     for (int j = 0; j < 4; ++j) { const int col = c0 + 4 * j;
;         const f32x4 x1 = (t[j] - R.st.x) * R.st.y * *(const LAS f32x4*)(cv + col) + *(const LAS f32x4*)(cv + 1024 + col);
.LBB0_856:
	s_add_i32 s13, s23, 1
	s_cmp_lg_u32 s23, 31
	s_waitcnt vmcnt(0)
	v_cvt_pk_f32_fp8_e32 v[192:193], v40
	v_cvt_pk_f32_fp8_sdwa v[194:195], v40 src0_sel:WORD_1
	v_cvt_pk_f32_fp8_e32 v[196:197], v41
	v_cvt_pk_f32_fp8_sdwa v[198:199], v41 src0_sel:WORD_1
	v_cvt_pk_f32_fp8_e32 v[200:201], v42
	v_cvt_pk_f32_fp8_sdwa v[202:203], v42 src0_sel:WORD_1
	v_cvt_pk_f32_fp8_e32 v[180:181], v43
	v_cvt_pk_f32_fp8_sdwa v[182:183], v43 src0_sel:WORD_1
	s_cselect_b32 s4, s13, 31
	v_cvt_pk_f32_fp8_e32 v[156:157], v36
	v_cvt_pk_f32_fp8_sdwa v[164:165], v36 src0_sel:WORD_1
	v_cvt_pk_f32_fp8_e32 v[158:159], v37
	v_cvt_pk_f32_fp8_sdwa v[172:173], v37 src0_sel:WORD_1
	v_cvt_pk_f32_fp8_e32 v[166:167], v38
	v_cvt_pk_f32_fp8_sdwa v[184:185], v38 src0_sel:WORD_1
	v_cvt_pk_f32_fp8_e32 v[174:175], v39
	v_cvt_pk_f32_fp8_sdwa v[190:191], v39 src0_sel:WORD_1
	s_add_i32 s4, s4, s12
	v_cvt_pk_f32_fp8_e32 v[160:161], v32
	v_cvt_pk_f32_fp8_sdwa v[162:163], v32 src0_sel:WORD_1
	v_cvt_pk_f32_fp8_e32 v[168:169], v33
	v_cvt_pk_f32_fp8_sdwa v[170:171], v33 src0_sel:WORD_1
	v_cvt_pk_f32_fp8_e32 v[176:177], v34
	v_cvt_pk_f32_fp8_sdwa v[178:179], v34 src0_sel:WORD_1
	v_cvt_pk_f32_fp8_e32 v[186:187], v35
	v_cvt_pk_f32_fp8_sdwa v[188:189], v35 src0_sel:WORD_1
	v_cvt_pk_f32_fp8_e32 v[140:141], v12
	v_cvt_pk_f32_fp8_sdwa v[144:145], v12 src0_sel:WORD_1
	v_cvt_pk_f32_fp8_e32 v[142:143], v13
	v_cvt_pk_f32_fp8_sdwa v[148:149], v13 src0_sel:WORD_1
	v_cvt_pk_f32_fp8_e32 v[146:147], v14
	v_cvt_pk_f32_fp8_sdwa v[152:153], v14 src0_sel:WORD_1
	v_cvt_pk_f32_fp8_e32 v[150:151], v15
	v_cvt_pk_f32_fp8_sdwa v[154:155], v15 src0_sel:WORD_1
	v_cvt_pk_f32_fp8_e32 v[96:97], v8
	v_cvt_pk_f32_fp8_sdwa v[112:113], v8 src0_sel:WORD_1
	v_cvt_pk_f32_fp8_e32 v[106:107], v9
	v_cvt_pk_f32_fp8_sdwa v[116:117], v9 src0_sel:WORD_1
	v_cvt_pk_f32_fp8_e32 v[114:115], v10
	v_cvt_pk_f32_fp8_sdwa v[120:121], v10 src0_sel:WORD_1
	v_cvt_pk_f32_fp8_e32 v[118:119], v11
	v_cvt_pk_f32_fp8_sdwa v[122:123], v11 src0_sel:WORD_1
	v_cvt_pk_f32_fp8_e32 v[98:99], v4
	v_cvt_pk_f32_fp8_sdwa v[100:101], v4 src0_sel:WORD_1
	v_cvt_pk_f32_fp8_e32 v[80:81], v5
	v_cvt_pk_f32_fp8_sdwa v[82:83], v5 src0_sel:WORD_1
	v_cvt_pk_f32_fp8_e32 v[84:85], v6
	v_cvt_pk_f32_fp8_sdwa v[86:87], v6 src0_sel:WORD_1
	v_cvt_pk_f32_fp8_e32 v[76:77], v7
	v_cvt_pk_f32_fp8_sdwa v[78:79], v7 src0_sel:WORD_1
	v_cvt_pk_f32_fp8_e32 v[32:33], v0
	v_cvt_pk_f32_fp8_sdwa v[36:37], v0 src0_sel:WORD_1
	v_cvt_pk_f32_fp8_e32 v[34:35], v1
	v_cvt_pk_f32_fp8_sdwa v[40:41], v1 src0_sel:WORD_1
	v_cvt_pk_f32_fp8_e32 v[38:39], v2
	v_cvt_pk_f32_fp8_sdwa v[56:57], v2 src0_sel:WORD_1
	v_cvt_pk_f32_fp8_e32 v[42:43], v3
	v_cvt_pk_f32_fp8_sdwa v[58:59], v3 src0_sel:WORD_1
	v_lshlrev_b32_e32 v2, 16, v24
	v_and_b32_e32 v3, 0xffff0000, v24
	v_lshlrev_b32_e32 v0, 16, v25
	v_and_b32_e32 v1, 0xffff0000, v25
	v_lshlrev_b32_e32 v6, 16, v26
	v_and_b32_e32 v7, 0xffff0000, v26
	v_lshlrev_b32_e32 v4, 16, v27
	v_and_b32_e32 v5, 0xffff0000, v27
	v_lshlrev_b32_e32 v8, 16, v20
	v_and_b32_e32 v9, 0xffff0000, v20
	v_lshlrev_b32_e32 v10, 16, v21
	v_and_b32_e32 v11, 0xffff0000, v21
	v_lshlrev_b32_e32 v12, 16, v22
	v_and_b32_e32 v13, 0xffff0000, v22
	v_lshlrev_b32_e32 v14, 16, v23
	v_and_b32_e32 v15, 0xffff0000, v23
	s_ashr_i32 s5, s4, 31
	v_sub_f32_e32 v1, v1, v136
	v_sub_f32_e32 v0, v0, v136
	v_sub_f32_e32 v3, v3, v136
	v_sub_f32_e32 v2, v2, v136
	v_sub_f32_e32 v5, v5, v136
	v_sub_f32_e32 v4, v4, v136
	v_sub_f32_e32 v7, v7, v136
	v_sub_f32_e32 v6, v6, v136
	v_sub_f32_e32 v9, v9, v136
	v_sub_f32_e32 v8, v8, v136
	v_sub_f32_e32 v11, v11, v136
	v_sub_f32_e32 v10, v10, v136
	v_sub_f32_e32 v13, v13, v136
	v_sub_f32_e32 v12, v12, v136
	v_sub_f32_e32 v15, v15, v136
	v_sub_f32_e32 v14, v14, v136
	s_lshl_b64 s[14:15], s[4:5], 13
	v_cvt_pk_f32_fp8_e32 v[60:61], v16
	v_cvt_pk_f32_fp8_sdwa v[62:63], v16 src0_sel:WORD_1
	v_cvt_pk_f32_fp8_e32 v[64:65], v17
	v_cvt_pk_f32_fp8_sdwa v[66:67], v17 src0_sel:WORD_1
	v_pk_mul_f32 v[132:133], v[136:137], v[2:3] op_sel:[1,0]
	v_pk_mul_f32 v[138:139], v[136:137], v[0:1] op_sel:[1,0]
	v_pk_mul_f32 v[128:129], v[136:137], v[6:7] op_sel:[1,0]
	v_pk_mul_f32 v[134:135], v[136:137], v[4:5] op_sel:[1,0]
	v_pk_mul_f32 v[124:125], v[136:137], v[10:11] op_sel:[1,0]
	v_pk_mul_f32 v[130:131], v[136:137], v[8:9] op_sel:[1,0]
	v_pk_mul_f32 v[126:127], v[136:137], v[14:15] op_sel:[1,0]
	v_pk_mul_f32 v[136:137], v[136:137], v[12:13] op_sel:[1,0]
	v_pk_add_f32 v[0:1], v[192:193], 0 op_sel_hi:[1,0]
	v_pk_add_f32 v[2:3], v[194:195], 0 op_sel_hi:[1,0]
	v_pk_add_f32 v[4:5], v[196:197], 0 op_sel_hi:[1,0]
	v_pk_add_f32 v[6:7], v[198:199], 0 op_sel_hi:[1,0]
	v_pk_add_f32 v[8:9], v[200:201], 0 op_sel_hi:[1,0]
	v_pk_add_f32 v[10:11], v[202:203], 0 op_sel_hi:[1,0]
	v_pk_add_f32 v[12:13], v[180:181], 0 op_sel_hi:[1,0]
	v_pk_add_f32 v[14:15], v[182:183], 0 op_sel_hi:[1,0]
	v_lshl_add_u64 v[16:17], v[46:47], 0, s[14:15]
	s_lshl_b64 s[24:25], s[4:5], 10
	s_lshl_b64 s[26:27], s[4:5], 11
	s_lshl_b64 s[4:5], s[4:5], 3
	v_pk_add_f32 v[2:3], v[2:3], v[164:165]
	v_pk_add_f32 v[0:1], v[0:1], v[156:157]
	v_pk_add_f32 v[6:7], v[6:7], v[172:173]
	v_pk_add_f32 v[4:5], v[4:5], v[158:159]
	v_pk_add_f32 v[10:11], v[10:11], v[184:185]
	v_pk_add_f32 v[8:9], v[8:9], v[166:167]
	v_pk_add_f32 v[14:15], v[14:15], v[190:191]
	v_pk_add_f32 v[12:13], v[12:13], v[174:175]
	v_add_co_u32_e32 v156, vcc, s20, v16
	v_cvt_pk_f32_fp8_e32 v[88:89], v28
	v_cvt_pk_f32_fp8_sdwa v[90:91], v28 src0_sel:WORD_1
	v_cvt_pk_f32_fp8_e32 v[92:93], v29
	v_cvt_pk_f32_fp8_sdwa v[94:95], v29 src0_sel:WORD_1
	v_cvt_pk_f32_fp8_e32 v[102:103], v30
	v_cvt_pk_f32_fp8_sdwa v[104:105], v30 src0_sel:WORD_1
	v_cvt_pk_f32_fp8_e32 v[108:109], v31
; #define LAS __attribute__((address_space(3)))
; __device__ __forceinline__ void final_load(RowRaw& R, const bf16_t* __restrict__ tb, const unsigned char* __restrict__ ybuf, const unsigned char* __restrict__ ysh, const float* __restrict__ stats, int row, int lane) {
;     const int c0 = lane * 16;
; #pragma unroll
;     for (int k = 0; k < TOPK; ++k) R.y[k] = __builtin_nontemporal_load((const u32x4*)(ybuf + ((size_t)row * TOPK + k) * D + c0));
;     R.y[8] = __builtin_nontemporal_load((const u32x4*)(ysh + (size_t)row * D + c0));
;     R.t[0] = __builtin_nontemporal_load((const u32x4*)(tb + (size_t)row * D + c0)); R.t[1] = __builtin_nontemporal_load((const u32x4*)(tb + (size_t)row * D + c0 + 8));
;     R.st = *(const f32x2*)(stats + 2 * (size_t)row);
; }
; __device__ __forceinline__ void final_row(float* __restrict__ out, const RowRaw& R, const LAS float* cv  , int row, int lane) {
;     asm volatile("" : "+v"(cv));
;     const int c0 = lane * 16;
;     f32x4 a[4], t[4], v[4]; float s = 0.f;
; #pragma unroll
;     for (int j = 0; j < 4; ++j) a[j] = (f32x4){0.f, 0.f, 0.f, 0.f};
; #pragma unroll
;     for (int k = 0; k < 9; ++k) { const unsigned w[4] = {R.y[k].x, R.y[k].y, R.y[k].z, R.y[k].w};
; #pragma unroll
;         for (int j = 0; j < 4; ++j) { const f32x2 lo = __builtin_amdgcn_cvt_pk_f32_fp8((int)w[j], false), hi = __builtin_amdgcn_cvt_pk_f32_fp8((int)w[j], true); a[j].x += lo.x; a[j].y += lo.y; a[j].z += hi.x; a[j].w += hi.y; } }
;     unpack_t16r(R.t[0], R.t[1], t);
; #pragma unroll
;     for (int j = 0; j < 4; ++j) { const int col = c0 + 4 * j;
;         const f32x4 x1 = (t[j] - R.st.x) * R.st.y * *(const LAS f32x4*)(cv + col) + *(const LAS f32x4*)(cv + 1024 + col);
;         v[j] = x1 * ALPHA + *(const LAS f32x4*)(cv + 4096 + col) * a[j] * YINV;
;         s += (v[j].x + v[j].y) + (v[j].z + v[j].w); }
	v_cvt_pk_f32_fp8_sdwa v[110:111], v31 src0_sel:WORD_1
	v_cvt_pk_f32_fp8_e32 v[68:69], v18
	v_cvt_pk_f32_fp8_sdwa v[70:71], v18 src0_sel:WORD_1
	v_cvt_pk_f32_fp8_e32 v[72:73], v19
	v_cvt_pk_f32_fp8_sdwa v[74:75], v19 src0_sel:WORD_1
	v_lshl_add_u64 v[18:19], v[48:49], 0, s[24:25]
	v_lshl_add_u64 v[24:25], v[50:51], 0, s[26:27]
	s_add_u32 s14, s16, s4
	v_pk_add_f32 v[28:29], v[0:1], v[160:161]
	v_pk_add_f32 v[30:31], v[2:3], v[162:163]
	v_pk_add_f32 v[158:159], v[4:5], v[168:169]
	v_pk_add_f32 v[160:161], v[6:7], v[170:171]
	v_pk_add_f32 v[162:163], v[8:9], v[176:177]
	v_pk_add_f32 v[164:165], v[10:11], v[178:179]
	v_pk_add_f32 v[166:167], v[12:13], v[186:187]
	v_pk_add_f32 v[168:169], v[14:15], v[188:189]
	global_load_dwordx4 v[0:3], v[16:17], off nt
	global_load_dwordx4 v[4:7], v[16:17], off offset:1024 nt
	global_load_dwordx4 v[8:11], v[16:17], off offset:2048 nt
	global_load_dwordx4 v[12:15], v[16:17], off offset:3072 nt
	v_addc_co_u32_e32 v157, vcc, 0, v17, vcc
	global_load_dwordx4 v[20:23], v[24:25], off offset:16 nt
	s_nop 0
	global_load_dwordx4 v[16:19], v[18:19], off nt
	s_nop 0
	global_load_dwordx4 v[24:27], v[24:25], off nt
	s_addc_u32 s15, s17, s5
	v_pk_add_f32 v[170:171], v[30:31], v[144:145]
	v_pk_add_f32 v[172:173], v[28:29], v[140:141]
	v_pk_add_f32 v[160:161], v[160:161], v[148:149]
	v_pk_add_f32 v[158:159], v[158:159], v[142:143]
	v_pk_add_f32 v[152:153], v[164:165], v[152:153]
	v_pk_add_f32 v[162:163], v[162:163], v[146:147]
	v_pk_add_f32 v[164:165], v[166:167], v[150:151]
	global_load_dwordx4 v[28:31], v[156:157], off nt
	global_load_dwordx4 v[140:143], v[156:157], off offset:1024 nt
	global_load_dwordx4 v[144:147], v[156:157], off offset:2048 nt
	global_load_dwordx4 v[148:151], v[156:157], off offset:3072 nt
	global_load_dwordx2 v[188:189], v45, s[14:15]
	v_mov_b32_e32 v207, 0
	v_pk_add_f32 v[154:155], v[168:169], v[154:155]
	v_pk_add_f32 v[88:89], v[172:173], v[88:89]
	v_pk_add_f32 v[90:91], v[170:171], v[90:91]
	v_pk_add_f32 v[92:93], v[158:159], v[92:93]
	v_pk_add_f32 v[94:95], v[160:161], v[94:95]
	v_pk_add_f32 v[102:103], v[162:163], v[102:103]
	v_pk_add_f32 v[104:105], v[152:153], v[104:105]
	v_pk_add_f32 v[108:109], v[164:165], v[108:109]
	v_pk_add_f32 v[110:111], v[154:155], v[110:111]
	v_lshl_add_u32 v184, v44, 2, v207
	v_pk_add_f32 v[112:113], v[90:91], v[112:113]
	v_pk_add_f32 v[96:97], v[88:89], v[96:97]
	v_pk_add_f32 v[152:153], v[94:95], v[116:117]
	v_pk_add_f32 v[154:155], v[92:93], v[106:107]
	v_pk_add_f32 v[156:157], v[104:105], v[120:121]
	v_pk_add_f32 v[158:159], v[102:103], v[114:115]
	v_pk_add_f32 v[122:123], v[110:111], v[122:123]
	v_pk_add_f32 v[160:161], v[108:109], v[118:119]
	ds_read_b128 v[88:91], v216
	ds_read_b128 v[92:95], v217
	ds_read_b128 v[102:105], v218
	ds_read_b128 v[106:109], v219
	v_pk_add_f32 v[190:191], v[96:97], v[98:99]
	v_pk_add_f32 v[100:101], v[112:113], v[100:101]
	ds_read_b128 v[96:99], v216 offset:4096
	ds_read_b128 v[110:113], v217 offset:4096
	ds_read_b128 v[114:117], v216 offset:16384
	ds_read_b128 v[118:121], v217 offset:16384
	v_pk_add_f32 v[192:193], v[154:155], v[80:81]
	v_pk_add_f32 v[194:195], v[152:153], v[82:83]
	v_pk_add_f32 v[196:197], v[158:159], v[84:85]
	v_pk_add_f32 v[198:199], v[156:157], v[86:87]
	ds_read_b128 v[80:83], v218 offset:4096
	ds_read_b128 v[84:87], v219 offset:4096
	ds_read_b128 v[152:155], v218 offset:16384
	ds_read_b128 v[156:159], v219 offset:16384
	v_pk_add_f32 v[36:37], v[100:101], v[36:37]
	v_pk_add_f32 v[32:33], v[190:191], v[32:33]
	v_pk_add_f32 v[40:41], v[194:195], v[40:41]
	v_pk_add_f32 v[34:35], v[192:193], v[34:35]
	v_pk_add_f32 v[32:33], v[32:33], v[60:61]
	v_pk_add_f32 v[36:37], v[36:37], v[62:63]
	v_pk_add_f32 v[34:35], v[34:35], v[64:65]
	v_pk_add_f32 v[40:41], v[40:41], v[66:67]
	v_pk_add_f32 v[200:201], v[160:161], v[76:77]
	v_pk_add_f32 v[122:123], v[122:123], v[78:79]
	s_waitcnt lgkmcnt(5)
	v_pk_mul_f32 v[36:37], v[36:37], v[116:117]
	v_pk_mul_f32 v[32:33], v[32:33], v[114:115]
	s_waitcnt lgkmcnt(4)
	v_pk_mul_f32 v[40:41], v[40:41], v[120:121]
	v_pk_mul_f32 v[34:35], v[34:35], v[118:119]
	v_pk_add_f32 v[56:57], v[198:199], v[56:57]
	v_pk_add_f32 v[38:39], v[196:197], v[38:39]
	v_pk_add_f32 v[58:59], v[122:123], v[58:59]
	v_pk_add_f32 v[42:43], v[200:201], v[42:43]
	v_pk_fma_f32 v[60:61], v[138:139], v[90:91], v[98:99]
	v_pk_fma_f32 v[62:63], v[132:133], v[88:89], v[96:97]
	v_pk_fma_f32 v[64:65], v[134:135], v[94:95], v[112:113]
	v_pk_fma_f32 v[66:67], v[128:129], v[92:93], v[110:111]
	v_pk_mul_f32 v[36:37], v[36:37], s[8:9] op_sel_hi:[1,0]
	v_pk_mul_f32 v[32:33], v[32:33], s[8:9] op_sel_hi:[1,0]
	v_pk_mul_f32 v[40:41], v[40:41], s[8:9] op_sel_hi:[1,0]
	v_pk_mul_f32 v[34:35], v[34:35], s[8:9] op_sel_hi:[1,0]
	v_pk_add_f32 v[38:39], v[38:39], v[68:69]
	v_pk_add_f32 v[56:57], v[56:57], v[70:71]
	v_pk_add_f32 v[42:43], v[42:43], v[72:73]
	v_pk_add_f32 v[58:59], v[58:59], v[74:75]
	v_pk_fma_f32 v[32:33], v[62:63], s[10:11], v[32:33] op_sel_hi:[1,0,1]
	v_pk_fma_f32 v[36:37], v[60:61], s[10:11], v[36:37] op_sel_hi:[1,0,1]
	v_pk_fma_f32 v[34:35], v[66:67], s[10:11], v[34:35] op_sel_hi:[1,0,1]
	v_pk_fma_f32 v[40:41], v[64:65], s[10:11], v[40:41] op_sel_hi:[1,0,1]
	s_waitcnt lgkmcnt(1)
	v_pk_mul_f32 v[56:57], v[56:57], v[154:155]
	v_pk_mul_f32 v[38:39], v[38:39], v[152:153]
	s_waitcnt lgkmcnt(0)
; #define LAS __attribute__((address_space(3)))
; __device__ __forceinline__ void final_row(float* __restrict__ out, const RowRaw& R, const LAS float* cv  , int row, int lane) {
;     ...
;     for (int j = 0; j < 4; ++j) { const int col = c0 + 4 * j;
;         const f32x4 x1 = (t[j] - R.st.x) * R.st.y * *(const LAS f32x4*)(cv + col) + *(const LAS f32x4*)(cv + 1024 + col);
;         v[j] = x1 * ALPHA + *(const LAS f32x4*)(cv + 4096 + col) * a[j] * YINV;
;         s += (v[j].x + v[j].y) + (v[j].z + v[j].w); }
;     const float mean = wave_sum(s) * (1.f / D); float s2 = 0.f;
; #pragma unroll
;     for (int j = 0; j < 4; ++j) { v[j] = v[j] - mean; s2 += (v[j].x * v[j].x + v[j].y * v[j].y) + (v[j].z * v[j].z + v[j].w * v[j].w); }
;     const float rstd = 1.f / sqrtf(wave_sum(s2) * (1.f / D) + LN_EPS);
; #pragma unroll
;     for (int j = 0; j < 4; ++j) { const int col = c0 + 4 * j;
;         *(f32x4*)(out + (size_t)row * D + col) = v[j] * rstd * *(const LAS f32x4*)(cv + 2048 + col) + *(const LAS f32x4*)(cv + 3072 + col); }
	v_pk_mul_f32 v[58:59], v[58:59], v[158:159]
	v_pk_mul_f32 v[42:43], v[42:43], v[156:157]
	v_pk_mov_b32 v[60:61], v[32:33], v[36:37] op_sel:[1,0]
	v_mov_b32_e32 v62, v32
	v_mov_b32_e32 v63, v37
	v_pk_mov_b32 v[64:65], v[34:35], v[40:41] op_sel:[1,0]
	v_mov_b32_e32 v66, v34
	v_mov_b32_e32 v67, v41
	v_pk_fma_f32 v[68:69], v[130:131], v[102:103], v[80:81]
	v_pk_fma_f32 v[70:71], v[124:125], v[104:105], v[82:83]
	v_pk_fma_f32 v[72:73], v[136:137], v[106:107], v[84:85]
	v_pk_fma_f32 v[74:75], v[126:127], v[108:109], v[86:87]
	v_pk_mul_f32 v[56:57], v[56:57], s[8:9] op_sel_hi:[1,0]
	v_pk_mul_f32 v[38:39], v[38:39], s[8:9] op_sel_hi:[1,0]
	v_pk_mul_f32 v[58:59], v[58:59], s[8:9] op_sel_hi:[1,0]
	v_pk_mul_f32 v[42:43], v[42:43], s[8:9] op_sel_hi:[1,0]
	v_pk_add_f32 v[60:61], v[60:61], v[62:63]
	v_pk_add_f32 v[62:63], v[64:65], v[66:67]
	v_pk_fma_f32 v[56:57], v[70:71], s[10:11], v[56:57] op_sel_hi:[1,0,1]
	v_pk_fma_f32 v[38:39], v[68:69], s[10:11], v[38:39] op_sel_hi:[1,0,1]
	v_pk_fma_f32 v[58:59], v[74:75], s[10:11], v[58:59] op_sel_hi:[1,0,1]
	v_pk_fma_f32 v[42:43], v[72:73], s[10:11], v[42:43] op_sel_hi:[1,0,1]
	v_add_f32_e32 v66, v60, v61
	v_pk_add_f32 v[60:61], v[62:63], v[62:63] op_sel:[0,1] op_sel_hi:[1,0]
	v_add_f32_e32 v68, v38, v39
	v_add_f32_e32 v70, v56, v57
	v_mov_b32_e32 v73, v42
	v_mov_b32_e32 v69, v58
	v_mov_b32_e32 v71, v59
	v_add_f32_e32 v72, 0, v66
	v_mov_b32_e32 v61, v43
	v_pk_add_f32 v[64:65], v[68:69], v[70:71]
	v_pk_add_f32 v[60:61], v[72:73], v[60:61]
	s_add_i32 s4, s18, s23
	v_pk_add_f32 v[60:61], v[60:61], v[64:65]
	s_ashr_i32 s5, s4, 31
	v_add_f32_e32 v60, v60, v61
	s_lshl_b64 s[4:5], s[4:5], 12
	s_mov_b32 s23, s13
	v_add_f32_dpp v60, v60, v60 quad_perm:[1,0,3,2] row_mask:0xf bank_mask:0xf bound_ctrl:1
	s_cmp_eq_u32 s13, 32
	v_lshl_add_u64 v[202:203], v[52:53], 0, s[4:5]
	v_lshl_add_u64 v[212:213], v[210:211], 0, s[4:5]
	v_add_f32_dpp v60, v60, v60 quad_perm:[2,3,0,1] row_mask:0xf bank_mask:0xf bound_ctrl:1
	ds_read_b128 v[76:79], v216 offset:8192
	ds_read_b128 v[160:163], v217 offset:8192
	ds_read_b128 v[164:167], v216 offset:12288
	ds_read_b128 v[168:171], v217 offset:12288
	ds_read_b128 v[172:175], v218 offset:8192
	ds_read_b128 v[176:179], v219 offset:8192
	ds_read_b128 v[180:183], v218 offset:12288
	ds_read_b128 v[184:187], v219 offset:12288
	v_add_f32_dpp v60, v60, v60 row_half_mirror row_mask:0xf bank_mask:0xf bound_ctrl:1
	s_waitcnt vmcnt(0)
; #define LAS __attribute__((address_space(3)))
; __device__ __forceinline__ void final_row(float* __restrict__ out, const RowRaw& R, const LAS float* cv  , int row, int lane) {
;     ...
;     const float mean = wave_sum(s) * (1.f / D); float s2 = 0.f;
; #pragma unroll
;     for (int j = 0; j < 4; ++j) { v[j] = v[j] - mean; s2 += (v[j].x * v[j].x + v[j].y * v[j].y) + (v[j].z * v[j].z + v[j].w * v[j].w); }
;     const float rstd = 1.f / sqrtf(wave_sum(s2) * (1.f / D) + LN_EPS);
; #pragma unroll
;     for (int j = 0; j < 4; ++j) { const int col = c0 + 4 * j;
;         *(f32x4*)(out + (size_t)row * D + col) = v[j] * rstd * *(const LAS f32x4*)(cv + 2048 + col) + *(const LAS f32x4*)(cv + 3072 + col); }
; __global__ void __launch_bounds__(NW * 64, 2) mk_fwd(Args args) {
;     ...
;             for (int i = 0; i < 32; ++i) {
;                 const RowRaw cur = nx;
;                 final_load(nx, (const bf16_t*)(ws + WS_TB), ybuf, ws + WS_YSH, (const float*)(ws + WS_STATS), r0 + (i < 31 ? i + 1 : i), lane);
;                 final_row(out, cur, cv, r0 + i, lane);
;             }
	v_mov_b64_e32 v[136:137], v[188:189]
	v_add_f32_dpp v60, v60, v60 row_mirror row_mask:0xf bank_mask:0xf bound_ctrl:1
	s_nop 0
	v_readlane_b32 s13, v60, 16
	v_readlane_b32 s14, v60, 48
	v_readlane_b32 s4, v60, 0
	v_readlane_b32 s5, v60, 32
	v_mov_b32_e32 v60, s13
	v_mov_b32_e32 v61, s14
	v_pk_add_f32 v[60:61], s[4:5], v[60:61]
	s_nop 0
	v_add_f32_e32 v60, v60, v61
	v_fmamk_f32 v33, v60, 0xba800000, v33
	v_fmac_f32_e32 v32, 0xba800000, v60
	v_fmamk_f32 v37, v60, 0xba800000, v37
	v_fmac_f32_e32 v36, 0xba800000, v60
	v_fmamk_f32 v35, v60, 0xba800000, v35
	v_fmac_f32_e32 v34, 0xba800000, v60
	v_fmamk_f32 v41, v60, 0xba800000, v41
	v_fmac_f32_e32 v40, 0xba800000, v60
	v_fmamk_f32 v39, v60, 0xba800000, v39
	v_fmac_f32_e32 v38, 0xba800000, v60
	v_fmamk_f32 v57, v60, 0xba800000, v57
	v_fmac_f32_e32 v56, 0xba800000, v60
	v_fmamk_f32 v59, v60, 0xba800000, v59
	v_fmac_f32_e32 v58, 0xba800000, v60
	v_fmamk_f32 v43, v60, 0xba800000, v43
	v_fmac_f32_e32 v42, 0xba800000, v60
	v_pk_mul_f32 v[60:61], v[36:37], v[36:37]
	v_pk_mul_f32 v[62:63], v[32:33], v[32:33]
	v_pk_mul_f32 v[64:65], v[40:41], v[40:41]
	v_pk_mul_f32 v[66:67], v[34:35], v[34:35]
	v_pk_mov_b32 v[72:73], v[62:63], v[60:61] op_sel:[1,0]
	v_mov_b32_e32 v63, v61
	v_pk_mov_b32 v[60:61], v[66:67], v[64:65] op_sel:[1,0]
	v_mov_b32_e32 v67, v65
	v_mul_f32_e32 v68, v38, v38
	v_mul_f32_e32 v70, v56, v56
	v_pk_add_f32 v[62:63], v[72:73], v[62:63]
	v_pk_add_f32 v[60:61], v[60:61], v[66:67]
	v_pk_fma_f32 v[64:65], v[38:39], v[38:39], v[68:69] op_sel_hi:[1,1,0]
	v_pk_fma_f32 v[68:69], v[56:57], v[56:57], v[70:71] op_sel_hi:[1,1,0]
	v_pk_add_f32 v[62:63], v[62:63], v[62:63] op_sel_hi:[0,1]
	v_pk_add_f32 v[60:61], v[60:61], v[60:61] op_sel_hi:[0,1]
	v_mul_f32_e32 v64, v42, v42
	v_mul_f32_e32 v68, v43, v43
	v_mul_f32_e32 v62, v58, v58
	v_mul_f32_e32 v60, v59, v59
	v_pk_add_f32 v[64:65], v[64:65], v[68:69]
	v_pk_add_f32 v[60:61], v[62:63], v[60:61]
	s_nop 0
	v_pk_add_f32 v[60:61], v[64:65], v[60:61]
	s_nop 0
	v_add_f32_e32 v60, v60, v61
	s_nop 1
	v_add_f32_dpp v60, v60, v60 quad_perm:[1,0,3,2] row_mask:0xf bank_mask:0xf bound_ctrl:1
	s_nop 1
	v_add_f32_dpp v60, v60, v60 quad_perm:[2,3,0,1] row_mask:0xf bank_mask:0xf bound_ctrl:1
	s_nop 1
	v_add_f32_dpp v60, v60, v60 row_half_mirror row_mask:0xf bank_mask:0xf bound_ctrl:1
	s_nop 1
	v_add_f32_dpp v60, v60, v60 row_mirror row_mask:0xf bank_mask:0xf bound_ctrl:1
	s_nop 0
	v_readlane_b32 s13, v60, 16
	v_readlane_b32 s14, v60, 48
	v_readlane_b32 s4, v60, 0
	v_readlane_b32 s5, v60, 32
	v_mov_b32_e32 v60, s13
	v_mov_b32_e32 v61, s14
	v_pk_add_f32 v[60:61], s[4:5], v[60:61]
	s_nop 0
	v_add_f32_e32 v60, v60, v61
	v_fmamk_f32 v60, v60, 0x3a800000, v205
	v_mul_f32_e32 v61, 0x4f800000, v60
	v_cmp_gt_f32_e32 vcc, s21, v60
	s_nop 1
	v_cndmask_b32_e32 v60, v60, v61, vcc
	v_sqrt_f32_e32 v61, v60
	s_nop 0
	v_add_u32_e32 v62, -1, v61
	v_add_u32_e32 v63, 1, v61
	v_fma_f32 v64, -v62, v61, v60
	v_fma_f32 v65, -v63, v61, v60
	v_cmp_ge_f32_e64 s[4:5], 0, v64
	s_nop 1
	v_cndmask_b32_e64 v61, v61, v62, s[4:5]
	v_cmp_lt_f32_e64 s[4:5], 0, v65
	s_nop 1
	v_cndmask_b32_e64 v61, v61, v63, s[4:5]
	v_mul_f32_e32 v62, 0x37800000, v61
	v_cndmask_b32_e32 v61, v61, v62, vcc
	v_cmp_class_f32_e32 vcc, v60, v206
	s_nop 1
	v_cndmask_b32_e32 v60, v61, v60, vcc
	v_div_scale_f32 v61, s[4:5], v60, v60, 1.0
	v_rcp_f32_e32 v63, v61
	v_div_scale_f32 v62, vcc, 1.0, v60, 1.0
	v_fma_f32 v64, -v61, v63, 1.0
	v_fmac_f32_e32 v63, v64, v63
	v_mul_f32_e32 v64, v62, v63
	v_fma_f32 v65, -v61, v64, v62
	v_fmac_f32_e32 v64, v65, v63
	v_fma_f32 v61, -v61, v64, v62
	v_div_fmas_f32 v61, v61, v63, v64
	v_div_fixup_f32 v60, v61, v60, 1.0
	v_pk_mul_f32 v[32:33], v[32:33], v[60:61] op_sel_hi:[1,0]
	v_pk_mul_f32 v[36:37], v[36:37], v[60:61] op_sel_hi:[1,0]
	v_pk_mul_f32 v[62:63], v[34:35], v[60:61] op_sel_hi:[1,0]
	v_pk_mul_f32 v[40:41], v[40:41], v[60:61] op_sel_hi:[1,0]
	v_pk_mul_f32 v[56:57], v[56:57], v[60:61] op_sel_hi:[1,0]
	v_pk_mul_f32 v[64:65], v[38:39], v[60:61] op_sel_hi:[1,0]
	v_pk_mul_f32 v[58:59], v[58:59], v[60:61] op_sel_hi:[1,0]
	v_pk_mul_f32 v[60:61], v[42:43], v[60:61] op_sel_hi:[1,0]
	s_waitcnt lgkmcnt(5)
	v_pk_fma_f32 v[34:35], v[78:79], v[36:37], v[166:167]
	v_pk_fma_f32 v[32:33], v[76:77], v[32:33], v[164:165]
	s_waitcnt lgkmcnt(4)
	v_pk_fma_f32 v[38:39], v[162:163], v[40:41], v[170:171]
	v_pk_fma_f32 v[36:37], v[160:161], v[62:63], v[168:169]
	s_waitcnt lgkmcnt(1)
	v_pk_fma_f32 v[40:41], v[172:173], v[64:65], v[180:181]
	v_pk_fma_f32 v[42:43], v[174:175], v[56:57], v[182:183]
	s_waitcnt lgkmcnt(0)
	v_pk_fma_f32 v[56:57], v[60:61], v[176:177], v[184:185]
	v_pk_fma_f32 v[58:59], v[58:59], v[178:179], v[186:187]
	ds_write_b128 v208, v[32:35]
	ds_write_b128 v208, v[36:39] offset:16
	ds_write_b128 v208, v[40:43] offset:32
	ds_write_b128 v208, v[56:59] offset:48
	ds_read_b128 v[32:35], v209
	ds_read_b128 v[36:39], v209 offset:1280
	ds_read_b128 v[40:43], v209 offset:2560
	ds_read_b128 v[56:59], v209 offset:3840
	s_waitcnt lgkmcnt(0)
	global_store_dwordx4 v[212:213], v[32:35], off
	global_store_dwordx4 v[212:213], v[36:39], off offset:1024
	global_store_dwordx4 v[212:213], v[40:43], off offset:2048
	global_store_dwordx4 v[212:213], v[56:59], off offset:3072
	v_mov_b64_e32 v[34:35], v[10:11]
	v_mov_b64_e32 v[38:39], v[6:7]
	v_mov_b64_e32 v[42:43], v[2:3]
	v_mov_b64_e32 v[32:33], v[8:9]
	v_mov_b64_e32 v[36:37], v[4:5]
	v_mov_b64_e32 v[40:41], v[0:1]
	v_mov_b64_e32 v[0:1], v[148:149]
	v_mov_b64_e32 v[4:5], v[144:145]
	v_mov_b64_e32 v[8:9], v[140:141]
	v_mov_b64_e32 v[2:3], v[150:151]
	v_mov_b64_e32 v[6:7], v[146:147]
	v_mov_b64_e32 v[10:11], v[142:143]
	s_cbranch_scc0 .LBB0_856
	s_add_i32 s44, s44, s9
	s_add_i32 s18, s18, s19
	s_cmpk_gt_i32 s44, 0xff
	s_cbranch_scc0 .LBB0_851
